# baseline (speedup 1.0000x reference)
_Z6scan_kPKDF16_S0_S0_S0_PKfPf:
	s_load_dwordx8 s[4:11], s[0:1], 0x0
	s_load_dwordx4 s[12:15], s[0:1], 0x20
	v_and_b32_e32 v1, 63, v0
	v_lshrrev_b32_e32 v2, 6, v0
	s_nop 1
	v_readfirstlane_b32 s16, v2
	s_lshr_b32 s17, s2, 7
	s_and_b32 s18, s2, 127
	s_lshl_b32 s18, s18, 2
	s_add_u32 s18, s18, s16
	s_lshl_b32 s19, s17, 9
	s_add_u32 s19, s19, s18
	s_mul_i32 s28, s16, 4608
	s_add_u32 s28, s28, 67584
	s_lshl_b32 s32, s16, 10
	s_add_u32 s33, s32, 0x1000
	s_add_u32 s34, s32, 0x2000
	s_add_u32 s35, s32, 0x3000
	s_mov_b32 s46, 0x200
	s_mov_b32 s47, 0
	s_mov_b32 s40, 0
	v_lshlrev_b32_e32 v2, 4, v1
	v_add_u32_e32 v3, 0x1000, v2
	v_add_u32_e32 v4, 0x2000, v2
	v_add_u32_e32 v5, 0x3000, v2
	v_lshlrev_b32_e32 v6, 2, v1
	v_lshlrev_b32_e32 v7, 1, v1
	v_and_b32_e32 v20, 7, v1
	v_lshlrev_b32_e32 v20, 1, v20
	v_add_u32_e32 v8, v2, v20
	v_add_u32_e32 v8, s28, v8
	v_and_b32_e32 v20, 3, v1
	v_bfe_u32 v21, v1, 3, 2
	v_lshl_add_u32 v20, v21, 2, v20
	v_lshrrev_b32_e32 v21, 5, v1
	v_bfe_u32 v22, v1, 2, 1
	v_bfe_u32 v23, v1, 4, 1
	v_cmp_eq_u32_e64 s[48:49], v21, v22
	v_cmp_eq_u32_e64 s[50:51], 0, v23
	s_nop 1
	s_and_b64 s[52:53], s[48:49], s[50:51]
	s_andn2_b64 s[54:55], s[48:49], s[50:51]
	v_mov_b32_e32 v24, 65536
	v_lshlrev_b32_e32 v25, 1, v20
	v_add_u32_e32 v25, s28, v25
	v_add_u32_e32 v26, 0x100, v25
	s_nop 1
	v_cndmask_b32_e64 v9, v24, v25, s[48:49]
	v_cndmask_b32_e64 v10, v24, v26, s[48:49]
	v_lshlrev_b32_e32 v25, 4, v20
	v_add_u32_e32 v25, s28, v25
	v_add_u32_e32 v25, 0x200, v25
	v_add_u32_e32 v26, 0x800, v25
	v_cndmask_b32_e64 v11, v24, v25, s[48:49]
	v_cndmask_b32_e64 v13, v24, v26, s[48:49]
	v_mov_b32_e32 v15, 1.0
	v_and_b32_e32 v89, 15, v1
	s_mov_b32 s42, 0xffff
	s_mov_b32 s43, 0
	v_xor_b32_e32 v86, 16, v1
	v_lshlrev_b32_e32 v86, 2, v86
	v_xor_b32_e32 v87, 32, v1
	v_lshlrev_b32_e32 v87, 2, v87
	s_waitcnt lgkmcnt(0)
	s_lshl_b32 s30, s19, 13
	s_add_u32 s24, s4, s30
	s_addc_u32 s25, s5, 0
	s_add_u32 s26, s6, s30
	s_addc_u32 s27, s7, 0
	s_lshl_b32 s30, s17, 19
	s_add_u32 s30, s30, s32
	s_add_u32 s20, s8, s30
	s_addc_u32 s21, s9, 0
	s_add_u32 s22, s10, s30
	s_addc_u32 s23, s11, 0
	s_lshl_b32 s30, s18, 8
	s_add_u32 s12, s12, s30
	s_addc_u32 s13, s13, 0
	global_load_dword v90, v6, s[12:13]
	global_load_ushort v18, v7, s[26:27]
	global_load_ushort v19, v7, s[26:27] offset:128
	s_lshl_b32 s30, s19, 14
	s_add_u32 s14, s14, s30
	s_addc_u32 s15, s15, 0
	v_and_b32_e32 v30, 15, v1
	v_lshlrev_b32_e32 v30, 2, v30
	v_mov_b32_e32 v31, 0
	v_lshl_add_u64 v[16:17], s[14:15], 0, v[30:31]
	v_mov_b32_e32 v36, 0
	v_mov_b32_e32 v37, 0
	v_mov_b32_e32 v38, 0
	v_mov_b32_e32 v39, 0
	v_add_u32_e32 v29, 65536, v2
	ds_write_b128 v29, v[36:39]
	ds_write_b128 v29, v[36:39] offset:1024
	v_add_u32_e32 v29, s28, v2
	ds_write_b128 v29, v[36:39] offset:512
	ds_write_b128 v29, v[36:39] offset:1536
	ds_write_b128 v29, v[36:39] offset:2560
	ds_write_b128 v29, v[36:39] offset:3584
	s_mov_b32 m0, s32
	s_nop 0
	global_load_lds_dwordx4 v2, s[20:21]
	s_add_i32 m0, s32, 32768
	s_nop 0
	global_load_lds_dwordx4 v2, s[22:23]
	s_mov_b32 m0, s33
	s_nop 0
	global_load_lds_dwordx4 v3, s[20:21]
	s_add_i32 m0, s33, 32768
	s_nop 0
	global_load_lds_dwordx4 v3, s[22:23]
	s_mov_b32 m0, s34
	s_nop 0
	global_load_lds_dwordx4 v4, s[20:21]
	s_add_i32 m0, s34, 32768
	s_nop 0
	global_load_lds_dwordx4 v4, s[22:23]
	s_mov_b32 m0, s35
	s_nop 0
	global_load_lds_dwordx4 v5, s[20:21]
	s_add_i32 m0, s35, 32768
	s_nop 0
	global_load_lds_dwordx4 v5, s[22:23]
	s_mov_b32 m0, s28
	s_nop 0
	global_load_lds_dword v6, s[24:25]
	s_add_u32 s20, s20, 0x4000
	s_addc_u32 s21, s21, 0
	s_add_u32 s22, s22, 0x4000
	s_addc_u32 s23, s23, 0
	s_add_u32 s24, s24, 0x100
	s_addc_u32 s25, s25, 0
	s_add_i32 m0, s32, 16384
	s_nop 0
	global_load_lds_dwordx4 v2, s[20:21]
	s_add_i32 m0, s32, 49152
	s_nop 0
	global_load_lds_dwordx4 v2, s[22:23]
	s_add_i32 m0, s33, 16384
	s_nop 0
	global_load_lds_dwordx4 v3, s[20:21]
	s_add_i32 m0, s33, 49152
	s_nop 0
	global_load_lds_dwordx4 v3, s[22:23]
	s_add_i32 m0, s34, 16384
	s_nop 0
	global_load_lds_dwordx4 v4, s[20:21]
	s_add_i32 m0, s34, 49152
	s_nop 0
	global_load_lds_dwordx4 v4, s[22:23]
	s_add_i32 m0, s35, 16384
	s_nop 0
	global_load_lds_dwordx4 v5, s[20:21]
	s_add_i32 m0, s35, 49152
	s_nop 0
	global_load_lds_dwordx4 v5, s[22:23]
	s_add_i32 m0, s28, 0x100
	s_nop 0
	global_load_lds_dword v6, s[24:25]
	s_add_u32 s20, s20, 0x4000
	s_addc_u32 s21, s21, 0
	s_add_u32 s22, s22, 0x4000
	s_addc_u32 s23, s23, 0
	s_add_u32 s24, s24, 0x100
	s_addc_u32 s25, s25, 0
	s_mov_b32 s3, 0x3fb8aa3b
	s_waitcnt vmcnt(20)
	v_mul_f32_e32 v91, 0x3fb8aa3b, v90
	v_fma_f32 v92, v90, s3, -v91
	v_rndne_f32_e32 v93, v91
	v_fmamk_f32 v92, v90, 0x32a5705f, v92
	v_sub_f32_e32 v91, v91, v93
	v_add_f32_e32 v91, v91, v92
	v_exp_f32_e32 v91, v91
	v_cvt_i32_f32_e32 v92, v93
	s_mov_b32 s3, 0xc2ce8ed0
	v_cmp_ngt_f32_e32 vcc, s3, v90
	s_mov_b32 s3, 0x42b17218
	v_ldexp_f32 v91, v91, v92
	v_cndmask_b32_e32 v91, 0, v91, vcc
	v_mov_b32_e32 v92, 0x7f800000
	v_cmp_nlt_f32_e32 vcc, s3, v90
	s_mov_b32 s3, 0xbfb8aa3b
	s_nop 1
	v_cndmask_b32_e32 v90, v92, v91, vcc
	v_mov_b32_e32 v93, 0
	s_nop 0
	v_fma_mixlo_f16 v93, v90, s3, 0
	v_and_b32_e32 v28, 0xffff, v93
	v_mov_b32_e32 v29, 0
	v_mov_b32_e32 v30, 0
	v_mov_b32_e32 v31, 0
	v_mov_b32_e32 v32, 0
	v_mov_b32_e32 v33, 0
	v_mov_b32_e32 v34, 0
	v_mov_b32_e32 v35, 0
	v_mov_b32_e32 v96, 0x1c00
	v_mov_b32_e32 v97, 0x1c000000
	v_cmp_eq_u32_e32 vcc, 0, v89
	s_nop 1
	v_cndmask_b32_e32 v20, 0, v96, vcc
	v_cmp_eq_u32_e32 vcc, 1, v89
	s_nop 1
	v_cndmask_b32_e32 v20, v20, v97, vcc
	v_cmp_eq_u32_e32 vcc, 2, v89
	s_nop 1
	v_cndmask_b32_e32 v21, 0, v96, vcc
	v_cmp_eq_u32_e32 vcc, 3, v89
	s_nop 1
	v_cndmask_b32_e32 v21, v21, v97, vcc
	v_cmp_eq_u32_e32 vcc, 4, v89
	s_nop 1
	v_cndmask_b32_e32 v22, 0, v96, vcc
	v_cmp_eq_u32_e32 vcc, 5, v89
	s_nop 1
	v_cndmask_b32_e32 v22, v22, v97, vcc
	v_cmp_eq_u32_e32 vcc, 6, v89
	s_nop 1
	v_cndmask_b32_e32 v23, 0, v96, vcc
	v_cmp_eq_u32_e32 vcc, 7, v89
	s_nop 1
	v_cndmask_b32_e32 v23, v23, v97, vcc
	v_cmp_eq_u32_e32 vcc, 8, v89
	s_nop 1
	v_cndmask_b32_e32 v24, 0, v96, vcc
	v_cmp_eq_u32_e32 vcc, 9, v89
	s_nop 1
	v_cndmask_b32_e32 v24, v24, v97, vcc
	v_cmp_eq_u32_e32 vcc, 10, v89
	s_nop 1
	v_cndmask_b32_e32 v25, 0, v96, vcc
	v_cmp_eq_u32_e32 vcc, 11, v89
	s_nop 1
	v_cndmask_b32_e32 v25, v25, v97, vcc
	v_cmp_eq_u32_e32 vcc, 12, v89
	s_nop 1
	v_cndmask_b32_e32 v26, 0, v96, vcc
	v_cmp_eq_u32_e32 vcc, 13, v89
	s_nop 1
	v_cndmask_b32_e32 v26, v26, v97, vcc
	v_cmp_eq_u32_e32 vcc, 14, v89
	s_nop 1
	v_cndmask_b32_e32 v27, 0, v96, vcc
	v_cmp_eq_u32_e32 vcc, 15, v89
	s_nop 1
	v_cndmask_b32_e32 v27, v27, v97, vcc
	v_mov_b32_e32 v195, 0
	v_mov_b32_e32 v85, 0
	v_mov_b32_e32 v88, 0
	v_mov_b32_e32 v84, 0
	v_mov_b32_e32 v68, 0
	v_mov_b32_e32 v69, 0
	v_mov_b32_e32 v70, 0
	v_mov_b32_e32 v71, 0
	v_mov_b32_e32 v72, 0
	v_mov_b32_e32 v73, 0
	v_mov_b32_e32 v74, 0
	v_mov_b32_e32 v75, 0
	v_mov_b32_e32 v76, 0
	v_mov_b32_e32 v77, 0
	v_mov_b32_e32 v78, 0
	v_mov_b32_e32 v79, 0
	v_mov_b32_e32 v80, 0
	v_mov_b32_e32 v81, 0
	v_mov_b32_e32 v82, 0
	v_mov_b32_e32 v83, 0
	s_waitcnt vmcnt(18)
	v_add_u32_e32 v8, 0x200, v8
	v_add_u32_e32 v94, 0x800, v8
	v_mov_b32_e32 v92, v2
	v_add_u32_e32 v93, 0x4000, v2
	s_mov_b32 s29, s28
	ds_write_b16 v8, v18
	ds_write_b16 v8, v19 offset:1024
	s_add_u32 s26, s26, 0x100
	s_addc_u32 s27, s27, 0
	global_load_ushort v18, v7, s[26:27]
	global_load_ushort v19, v7, s[26:27] offset:128
	s_add_u32 s26, s26, 0x100
	s_addc_u32 s27, s27, 0
	s_waitcnt vmcnt(0)
	s_waitcnt lgkmcnt(0)
	s_barrier
	ds_read_b128 v[52:55], v92 offset:32768
	ds_read_b128 v[56:59], v92 offset:33792
	ds_read_u16 v32, v9 offset:0
	ds_read_b128 v[36:39], v11 offset:0
	ds_read_b128 v[44:47], v92 offset:0
	ds_read_b128 v[48:51], v92 offset:1024
	s_waitcnt lgkmcnt(0)
	v_mfma_f32_32x32x16_f16 v[98:113], v[32:35], v[28:31], 0
	v_mfma_f32_32x32x16_f16 v[132:147], v[36:39], v[44:47], 0
	v_mfma_f32_32x32x16_f16 v[164:179], v[36:39], v[48:51], 0
	ds_read_u16 v32, v9 offset:32
	ds_read_b128 v[36:39], v11 offset:256
	ds_read_b128 v[44:47], v92 offset:2048
	ds_read_b128 v[48:51], v92 offset:3072
	s_nop 15
	s_nop 15
.Lscan_loop:
	v_exp_f32_e32 v98, v98
	v_exp_f32_e32 v99, v99
	v_mfma_f32_16x16x32_f16 v[80:83], v[72:75], v[24:27], v[80:83]
	ds_read_b128 v[60:63], v92 offset:34816
	ds_bpermute_b32 v90, v87, v85
	s_waitcnt lgkmcnt(2)
	v_exp_f32_e32 v100, v100
	v_exp_f32_e32 v101, v101
	v_mfma_f32_32x32x16_f16 v[114:129], v[32:35], v[28:31], 0
	ds_read_u16 v32, v9 offset:64
	ds_read_b128 v[64:67], v92 offset:35840
	v_fmac_f32_e32 v132, v98, v195
	v_exp_f32_e32 v102, v102
	v_fmac_f32_e32 v133, v99, v132
	v_exp_f32_e32 v103, v103
	v_fmac_f32_e32 v134, v100, v133
	v_cvt_pkrtz_f16_f32 v68, v132, v133
	v_exp_f32_e32 v104, v104
	v_fmac_f32_e32 v135, v101, v134
	v_pk_mul_f16 v68, v52, v68
	v_exp_f32_e32 v105, v105
	v_add_f32_e32 v84, v80, v81
	v_add_f32_e32 v91, v82, v83
	v_fmac_f32_e32 v136, v102, v135
	v_add_f32_e32 v84, v84, v91
	v_cvt_pkrtz_f16_f32 v69, v134, v135
	v_mfma_f32_32x32x16_f16 v[148:163], v[36:39], v[44:47], 0
	ds_read_b128 v[44:47], v92 offset:4096
	ds_bpermute_b32 v89, v86, v84
	v_exp_f32_e32 v106, v106
	v_fmac_f32_e32 v137, v103, v136
	v_pk_mul_f16 v69, v53, v69
	v_exp_f32_e32 v107, v107
	v_fmac_f32_e32 v138, v104, v137
	v_cvt_pkrtz_f16_f32 v70, v136, v137
	v_exp_f32_e32 v108, v108
	v_fmac_f32_e32 v139, v105, v138
	v_pk_mul_f16 v70, v54, v70
	v_exp_f32_e32 v109, v109
	v_mfma_f32_32x32x16_f16 v[180:195], v[36:39], v[48:51], 0
	ds_read_b128 v[36:39], v11 offset:512
	ds_read_b128 v[48:51], v92 offset:5120
	v_cvt_pkrtz_f16_f32 v71, v138, v139
	v_fmac_f32_e32 v172, v106, v139
	v_pk_mul_f16 v71, v55, v71
	v_exp_f32_e32 v110, v110
	v_fmac_f32_e32 v173, v107, v172
	v_mfma_f32_16x16x32_f16 v[76:79], v[68:71], v[20:23], 0
	v_cvt_pkrtz_f16_f32 v72, v172, v173
	v_exp_f32_e32 v111, v111
	v_fmac_f32_e32 v174, v108, v173
	v_pk_mul_f16 v72, v56, v72
	v_fmac_f32_e32 v175, v109, v174
	v_exp_f32_e32 v112, v112
	v_cvt_pkrtz_f16_f32 v73, v174, v175
	v_fmac_f32_e32 v176, v110, v175
	v_pk_mul_f16 v73, v57, v73
	v_fmac_f32_e32 v177, v111, v176
	v_exp_f32_e32 v113, v113
	v_cvt_pkrtz_f16_f32 v74, v176, v177
	v_fmac_f32_e32 v178, v112, v177
	v_pk_mul_f16 v74, v58, v74
	s_waitcnt lgkmcnt(2)
	v_add_f32_e32 v202, v85, v90
	v_fmac_f32_e32 v179, v113, v178
	v_add_f32_e32 v88, v84, v89
	v_cvt_pkrtz_f16_f32 v75, v178, v179
	v_pk_mul_f16 v75, v59, v75
	v_exp_f32_e32 v114, v114
	v_exp_f32_e32 v115, v115
	v_mfma_f32_16x16x32_f16 v[76:79], v[72:75], v[24:27], v[76:79]
	ds_read_b128 v[52:55], v92 offset:36864
	ds_bpermute_b32 v90, v87, v88
	s_waitcnt lgkmcnt(2)
	v_exp_f32_e32 v116, v116
	v_exp_f32_e32 v117, v117
	v_mfma_f32_32x32x16_f16 v[98:113], v[32:35], v[28:31], 0
	ds_read_u16 v32, v9 offset:96
	ds_read_b128 v[56:59], v92 offset:37888
	v_fmac_f32_e32 v148, v114, v179
	v_exp_f32_e32 v118, v118
	v_fmac_f32_e32 v149, v115, v148
	v_exp_f32_e32 v119, v119
	v_fmac_f32_e32 v150, v116, v149
	v_cvt_pkrtz_f16_f32 v68, v148, v149
	v_exp_f32_e32 v120, v120
	v_fmac_f32_e32 v151, v117, v150
	v_pk_mul_f16 v68, v60, v68
	v_exp_f32_e32 v121, v121
	v_add_f32_e32 v84, v76, v77
	v_add_f32_e32 v91, v78, v79
	v_fmac_f32_e32 v152, v118, v151
	v_add_f32_e32 v84, v84, v91
	v_cvt_pkrtz_f16_f32 v69, v150, v151
	v_mfma_f32_32x32x16_f16 v[132:147], v[36:39], v[44:47], 0
	ds_read_b128 v[44:47], v92 offset:6144
	ds_bpermute_b32 v89, v86, v84
	v_exp_f32_e32 v122, v122
	v_fmac_f32_e32 v153, v119, v152
	v_pk_mul_f16 v69, v61, v69
	v_exp_f32_e32 v123, v123
	v_fmac_f32_e32 v154, v120, v153
	v_cvt_pkrtz_f16_f32 v70, v152, v153
	v_exp_f32_e32 v124, v124
	v_fmac_f32_e32 v155, v121, v154
	v_pk_mul_f16 v70, v62, v70
	v_exp_f32_e32 v125, v125
	v_mfma_f32_32x32x16_f16 v[164:179], v[36:39], v[48:51], 0
	ds_read_b128 v[36:39], v11 offset:768
	ds_read_b128 v[48:51], v92 offset:7168
	v_cvt_pkrtz_f16_f32 v71, v154, v155
	v_fmac_f32_e32 v188, v122, v155
	v_pk_mul_f16 v71, v63, v71
	v_exp_f32_e32 v126, v126
	v_fmac_f32_e32 v189, v123, v188
	v_mfma_f32_16x16x32_f16 v[80:83], v[68:71], v[20:23], 0
	v_cvt_pkrtz_f16_f32 v72, v188, v189
	v_exp_f32_e32 v127, v127
	v_fmac_f32_e32 v190, v124, v189
	v_pk_mul_f16 v72, v64, v72
	v_fmac_f32_e32 v191, v125, v190
	v_exp_f32_e32 v128, v128
	v_cvt_pkrtz_f16_f32 v73, v190, v191
	v_fmac_f32_e32 v192, v126, v191
	v_pk_mul_f16 v73, v65, v73
	v_fmac_f32_e32 v193, v127, v192
	v_exp_f32_e32 v129, v129
	v_cvt_pkrtz_f16_f32 v74, v192, v193
	v_fmac_f32_e32 v194, v128, v193
	v_pk_mul_f16 v74, v66, v74
	s_waitcnt lgkmcnt(2)
	v_add_f32_e32 v203, v88, v90
	v_fmac_f32_e32 v195, v129, v194
	v_add_f32_e32 v85, v84, v89
	v_cvt_pkrtz_f16_f32 v75, v194, v195
	v_pk_mul_f16 v75, v67, v75
	v_exp_f32_e32 v98, v98
	v_exp_f32_e32 v99, v99
	v_mfma_f32_16x16x32_f16 v[80:83], v[72:75], v[24:27], v[80:83]
	ds_read_b128 v[60:63], v92 offset:38912
	ds_bpermute_b32 v90, v87, v85
	s_waitcnt lgkmcnt(2)
	v_exp_f32_e32 v100, v100
	v_exp_f32_e32 v101, v101
	v_mfma_f32_32x32x16_f16 v[114:129], v[32:35], v[28:31], 0
	ds_read_u16 v32, v9 offset:128
	ds_read_b128 v[64:67], v92 offset:39936
	v_fmac_f32_e32 v132, v98, v195
	v_exp_f32_e32 v102, v102
	v_fmac_f32_e32 v133, v99, v132
	v_exp_f32_e32 v103, v103
	v_fmac_f32_e32 v134, v100, v133
	v_cvt_pkrtz_f16_f32 v68, v132, v133
	v_exp_f32_e32 v104, v104
	v_fmac_f32_e32 v135, v101, v134
	v_pk_mul_f16 v68, v52, v68
	v_exp_f32_e32 v105, v105
	v_add_f32_e32 v84, v80, v81
	v_add_f32_e32 v91, v82, v83
	v_fmac_f32_e32 v136, v102, v135
	v_add_f32_e32 v84, v84, v91
	v_cvt_pkrtz_f16_f32 v69, v134, v135
	v_mfma_f32_32x32x16_f16 v[148:163], v[36:39], v[44:47], 0
	ds_read_b128 v[44:47], v92 offset:8192
	ds_bpermute_b32 v89, v86, v84
	v_exp_f32_e32 v106, v106
	v_fmac_f32_e32 v137, v103, v136
	v_pk_mul_f16 v69, v53, v69
	v_exp_f32_e32 v107, v107
	v_fmac_f32_e32 v138, v104, v137
	v_cvt_pkrtz_f16_f32 v70, v136, v137
	v_exp_f32_e32 v108, v108
	v_fmac_f32_e32 v139, v105, v138
	v_pk_mul_f16 v70, v54, v70
	v_exp_f32_e32 v109, v109
	v_mfma_f32_32x32x16_f16 v[180:195], v[36:39], v[48:51], 0
	ds_read_b128 v[36:39], v11 offset:1024
	ds_read_b128 v[48:51], v92 offset:9216
	v_cvt_pkrtz_f16_f32 v71, v138, v139
	v_fmac_f32_e32 v172, v106, v139
	v_pk_mul_f16 v71, v55, v71
	v_exp_f32_e32 v110, v110
	v_fmac_f32_e32 v173, v107, v172
	v_mfma_f32_16x16x32_f16 v[76:79], v[68:71], v[20:23], 0
	v_cvt_pkrtz_f16_f32 v72, v172, v173
	v_exp_f32_e32 v111, v111
	v_fmac_f32_e32 v174, v108, v173
	v_pk_mul_f16 v72, v56, v72
	v_fmac_f32_e32 v175, v109, v174
	v_exp_f32_e32 v112, v112
	v_cvt_pkrtz_f16_f32 v73, v174, v175
	v_fmac_f32_e32 v176, v110, v175
	v_pk_mul_f16 v73, v57, v73
	v_fmac_f32_e32 v177, v111, v176
	v_exp_f32_e32 v113, v113
	v_cvt_pkrtz_f16_f32 v74, v176, v177
	v_fmac_f32_e32 v178, v112, v177
	v_pk_mul_f16 v74, v58, v74
	s_waitcnt lgkmcnt(2)
	v_add_f32_e32 v196, v85, v90
	v_fmac_f32_e32 v179, v113, v178
	v_add_f32_e32 v88, v84, v89
	v_cvt_pkrtz_f16_f32 v75, v178, v179
	v_pk_mul_f16 v75, v59, v75
	v_exp_f32_e32 v114, v114
	v_exp_f32_e32 v115, v115
	v_mfma_f32_16x16x32_f16 v[76:79], v[72:75], v[24:27], v[76:79]
	ds_read_b128 v[52:55], v92 offset:40960
	ds_bpermute_b32 v90, v87, v88
	s_waitcnt lgkmcnt(2)
	v_exp_f32_e32 v116, v116
	v_exp_f32_e32 v117, v117
	v_mfma_f32_32x32x16_f16 v[98:113], v[32:35], v[28:31], 0
	ds_read_u16 v32, v9 offset:160
	ds_read_b128 v[56:59], v92 offset:41984
	v_fmac_f32_e32 v148, v114, v179
	v_exp_f32_e32 v118, v118
	v_fmac_f32_e32 v149, v115, v148
	v_exp_f32_e32 v119, v119
	v_fmac_f32_e32 v150, v116, v149
	v_cvt_pkrtz_f16_f32 v68, v148, v149
	v_exp_f32_e32 v120, v120
	v_fmac_f32_e32 v151, v117, v150
	v_pk_mul_f16 v68, v60, v68
	v_exp_f32_e32 v121, v121
	v_add_f32_e32 v84, v76, v77
	v_add_f32_e32 v91, v78, v79
	v_fmac_f32_e32 v152, v118, v151
	v_add_f32_e32 v84, v84, v91
	v_cvt_pkrtz_f16_f32 v69, v150, v151
	v_mfma_f32_32x32x16_f16 v[132:147], v[36:39], v[44:47], 0
	ds_read_b128 v[44:47], v92 offset:10240
	ds_bpermute_b32 v89, v86, v84
	v_exp_f32_e32 v122, v122
	v_fmac_f32_e32 v153, v119, v152
	v_pk_mul_f16 v69, v61, v69
	v_exp_f32_e32 v123, v123
	v_fmac_f32_e32 v154, v120, v153
	v_cvt_pkrtz_f16_f32 v70, v152, v153
	v_exp_f32_e32 v124, v124
	v_fmac_f32_e32 v155, v121, v154
	v_pk_mul_f16 v70, v62, v70
	v_exp_f32_e32 v125, v125
	v_mfma_f32_32x32x16_f16 v[164:179], v[36:39], v[48:51], 0
	ds_read_b128 v[36:39], v11 offset:1280
	ds_read_b128 v[48:51], v92 offset:11264
	v_cvt_pkrtz_f16_f32 v71, v154, v155
	v_fmac_f32_e32 v188, v122, v155
	v_pk_mul_f16 v71, v63, v71
	v_exp_f32_e32 v126, v126
	v_fmac_f32_e32 v189, v123, v188
	v_mfma_f32_16x16x32_f16 v[80:83], v[68:71], v[20:23], 0
	v_cvt_pkrtz_f16_f32 v72, v188, v189
	v_exp_f32_e32 v127, v127
	v_fmac_f32_e32 v190, v124, v189
	v_pk_mul_f16 v72, v64, v72
	v_fmac_f32_e32 v191, v125, v190
	v_exp_f32_e32 v128, v128
	v_cvt_pkrtz_f16_f32 v73, v190, v191
	v_fmac_f32_e32 v192, v126, v191
	v_pk_mul_f16 v73, v65, v73
	v_fmac_f32_e32 v193, v127, v192
	v_exp_f32_e32 v129, v129
	v_cvt_pkrtz_f16_f32 v74, v192, v193
	v_fmac_f32_e32 v194, v128, v193
	v_pk_mul_f16 v74, v66, v74
	s_waitcnt lgkmcnt(2)
	v_add_f32_e32 v197, v88, v90
	v_fmac_f32_e32 v195, v129, v194
	v_add_f32_e32 v85, v84, v89
	v_cvt_pkrtz_f16_f32 v75, v194, v195
	v_pk_mul_f16 v75, v67, v75
	v_exp_f32_e32 v98, v98
	v_exp_f32_e32 v99, v99
	v_mfma_f32_16x16x32_f16 v[80:83], v[72:75], v[24:27], v[80:83]
	ds_read_b128 v[60:63], v92 offset:43008
	ds_bpermute_b32 v90, v87, v85
	s_waitcnt lgkmcnt(2)
	v_exp_f32_e32 v100, v100
	v_exp_f32_e32 v101, v101
	v_mfma_f32_32x32x16_f16 v[114:129], v[32:35], v[28:31], 0
	ds_read_u16 v32, v9 offset:192
	ds_read_b128 v[64:67], v92 offset:44032
	v_fmac_f32_e32 v132, v98, v195
	v_exp_f32_e32 v102, v102
	v_fmac_f32_e32 v133, v99, v132
	v_exp_f32_e32 v103, v103
	v_fmac_f32_e32 v134, v100, v133
	v_cvt_pkrtz_f16_f32 v68, v132, v133
	v_exp_f32_e32 v104, v104
	v_fmac_f32_e32 v135, v101, v134
	v_pk_mul_f16 v68, v52, v68
	v_exp_f32_e32 v105, v105
	v_add_f32_e32 v84, v80, v81
	v_add_f32_e32 v91, v82, v83
	v_fmac_f32_e32 v136, v102, v135
	v_add_f32_e32 v84, v84, v91
	v_cvt_pkrtz_f16_f32 v69, v134, v135
	v_mfma_f32_32x32x16_f16 v[148:163], v[36:39], v[44:47], 0
	ds_read_b128 v[44:47], v92 offset:12288
	ds_bpermute_b32 v89, v86, v84
	v_exp_f32_e32 v106, v106
	v_fmac_f32_e32 v137, v103, v136
	v_pk_mul_f16 v69, v53, v69
	v_exp_f32_e32 v107, v107
	v_fmac_f32_e32 v138, v104, v137
	v_cvt_pkrtz_f16_f32 v70, v136, v137
	v_exp_f32_e32 v108, v108
	v_fmac_f32_e32 v139, v105, v138
	v_pk_mul_f16 v70, v54, v70
	v_exp_f32_e32 v109, v109
	v_mfma_f32_32x32x16_f16 v[180:195], v[36:39], v[48:51], 0
	ds_read_b128 v[36:39], v11 offset:1536
	ds_read_b128 v[48:51], v92 offset:13312
	v_cvt_pkrtz_f16_f32 v71, v138, v139
	v_fmac_f32_e32 v172, v106, v139
	v_pk_mul_f16 v71, v55, v71
	v_exp_f32_e32 v110, v110
	v_fmac_f32_e32 v173, v107, v172
	v_mfma_f32_16x16x32_f16 v[76:79], v[68:71], v[20:23], 0
	v_cvt_pkrtz_f16_f32 v72, v172, v173
	v_exp_f32_e32 v111, v111
	v_fmac_f32_e32 v174, v108, v173
	v_pk_mul_f16 v72, v56, v72
	v_fmac_f32_e32 v175, v109, v174
	v_exp_f32_e32 v112, v112
	v_cvt_pkrtz_f16_f32 v73, v174, v175
	v_fmac_f32_e32 v176, v110, v175
	v_pk_mul_f16 v73, v57, v73
	v_fmac_f32_e32 v177, v111, v176
	v_exp_f32_e32 v113, v113
	v_cvt_pkrtz_f16_f32 v74, v176, v177
	v_fmac_f32_e32 v178, v112, v177
	v_pk_mul_f16 v74, v58, v74
	s_waitcnt lgkmcnt(2)
	v_add_f32_e32 v198, v85, v90
	v_fmac_f32_e32 v179, v113, v178
	v_add_f32_e32 v88, v84, v89
	v_cvt_pkrtz_f16_f32 v75, v178, v179
	v_pk_mul_f16 v75, v59, v75
	v_exp_f32_e32 v114, v114
	v_exp_f32_e32 v115, v115
	v_mfma_f32_16x16x32_f16 v[76:79], v[72:75], v[24:27], v[76:79]
	ds_read_b128 v[52:55], v92 offset:45056
	ds_bpermute_b32 v90, v87, v88
	s_waitcnt lgkmcnt(2)
	s_waitcnt vmcnt(0)
	ds_write_b16 v94, v18
	ds_write_b16 v94, v19 offset:1024
	ds_read_b128 v[204:207], v92 offset:47104
	ds_read_b128 v[208:211], v92 offset:48128
	v_exp_f32_e32 v116, v116
	v_exp_f32_e32 v117, v117
	v_mfma_f32_32x32x16_f16 v[98:113], v[32:35], v[28:31], 0
	ds_read_u16 v32, v9 offset:224
	ds_read_b128 v[56:59], v92 offset:46080
	v_fmac_f32_e32 v148, v114, v179
	v_exp_f32_e32 v118, v118
	v_fmac_f32_e32 v149, v115, v148
	v_exp_f32_e32 v119, v119
	v_fmac_f32_e32 v150, v116, v149
	v_cvt_pkrtz_f16_f32 v68, v148, v149
	v_exp_f32_e32 v120, v120
	v_fmac_f32_e32 v151, v117, v150
	v_pk_mul_f16 v68, v60, v68
	v_exp_f32_e32 v121, v121
	v_add_f32_e32 v84, v76, v77
	v_add_f32_e32 v91, v78, v79
	v_fmac_f32_e32 v152, v118, v151
	v_add_f32_e32 v84, v84, v91
	v_cvt_pkrtz_f16_f32 v69, v150, v151
	v_mfma_f32_32x32x16_f16 v[132:147], v[36:39], v[44:47], 0
	ds_read_b128 v[44:47], v92 offset:14336
	ds_bpermute_b32 v89, v86, v84
	v_exp_f32_e32 v122, v122
	v_fmac_f32_e32 v153, v119, v152
	v_pk_mul_f16 v69, v61, v69
	v_exp_f32_e32 v123, v123
	v_fmac_f32_e32 v154, v120, v153
	v_cvt_pkrtz_f16_f32 v70, v152, v153
	v_exp_f32_e32 v124, v124
	v_fmac_f32_e32 v155, v121, v154
	v_pk_mul_f16 v70, v62, v70
	v_exp_f32_e32 v125, v125
	v_mfma_f32_32x32x16_f16 v[164:179], v[36:39], v[48:51], 0
	ds_read_b128 v[36:39], v11 offset:1792
	ds_read_b128 v[48:51], v92 offset:15360
	v_cvt_pkrtz_f16_f32 v71, v154, v155
	v_fmac_f32_e32 v188, v122, v155
	v_pk_mul_f16 v71, v63, v71
	v_exp_f32_e32 v126, v126
	v_fmac_f32_e32 v189, v123, v188
	v_mfma_f32_16x16x32_f16 v[80:83], v[68:71], v[20:23], 0
	v_cvt_pkrtz_f16_f32 v72, v188, v189
	v_exp_f32_e32 v127, v127
	v_fmac_f32_e32 v190, v124, v189
	v_pk_mul_f16 v72, v64, v72
	v_fmac_f32_e32 v191, v125, v190
	v_exp_f32_e32 v128, v128
	v_cvt_pkrtz_f16_f32 v73, v190, v191
	v_fmac_f32_e32 v192, v126, v191
	v_pk_mul_f16 v73, v65, v73
	v_fmac_f32_e32 v193, v127, v192
	v_exp_f32_e32 v129, v129
	v_cvt_pkrtz_f16_f32 v74, v192, v193
	v_fmac_f32_e32 v194, v128, v193
	v_pk_mul_f16 v74, v66, v74
	s_waitcnt lgkmcnt(2)
	v_add_f32_e32 v199, v88, v90
	v_fmac_f32_e32 v195, v129, v194
	v_add_f32_e32 v85, v84, v89
	v_cvt_pkrtz_f16_f32 v75, v194, v195
	v_pk_mul_f16 v75, v67, v75
	v_exp_f32_e32 v98, v98
	v_exp_f32_e32 v99, v99
	v_mfma_f32_16x16x32_f16 v[80:83], v[72:75], v[24:27], v[80:83]
	s_waitcnt lgkmcnt(0)
	s_barrier
	ds_bpermute_b32 v90, v87, v85
	v_exp_f32_e32 v100, v100
	v_exp_f32_e32 v101, v101
	v_mfma_f32_32x32x16_f16 v[114:129], v[32:35], v[28:31], 0
	s_mov_b32 m0, s32
	ds_read_u16 v32, v10 offset:0
	global_load_lds_dwordx4 v2, s[20:21]
	v_fmac_f32_e32 v132, v98, v195
	v_exp_f32_e32 v102, v102
	v_fmac_f32_e32 v133, v99, v132
	v_exp_f32_e32 v103, v103
	v_fmac_f32_e32 v134, v100, v133
	v_cvt_pkrtz_f16_f32 v68, v132, v133
	v_exp_f32_e32 v104, v104
	v_fmac_f32_e32 v135, v101, v134
	v_pk_mul_f16 v68, v52, v68
	v_exp_f32_e32 v105, v105
	v_add_f32_e32 v84, v80, v81
	v_add_f32_e32 v91, v82, v83
	v_fmac_f32_e32 v136, v102, v135
	v_add_f32_e32 v84, v84, v91
	v_cvt_pkrtz_f16_f32 v69, v134, v135
	v_mfma_f32_32x32x16_f16 v[148:163], v[36:39], v[44:47], 0
	ds_read_b128 v[44:47], v93 offset:0
	ds_bpermute_b32 v89, v86, v84
	s_add_i32 m0, s32, 32768
	s_nop 0
	global_load_lds_dwordx4 v2, s[22:23]
	v_exp_f32_e32 v106, v106
	v_fmac_f32_e32 v137, v103, v136
	v_pk_mul_f16 v69, v53, v69
	v_exp_f32_e32 v107, v107
	v_fmac_f32_e32 v138, v104, v137
	v_cvt_pkrtz_f16_f32 v70, v136, v137
	v_exp_f32_e32 v108, v108
	v_fmac_f32_e32 v139, v105, v138
	v_pk_mul_f16 v70, v54, v70
	v_exp_f32_e32 v109, v109
	v_mfma_f32_32x32x16_f16 v[180:195], v[36:39], v[48:51], 0
	ds_read_b128 v[36:39], v13 offset:0
	s_mov_b32 m0, s33
	ds_read_b128 v[48:51], v93 offset:1024
	global_load_lds_dwordx4 v3, s[20:21]
	v_cvt_pkrtz_f16_f32 v71, v138, v139
	v_fmac_f32_e32 v172, v106, v139
	v_pk_mul_f16 v71, v55, v71
	v_exp_f32_e32 v110, v110
	v_fmac_f32_e32 v173, v107, v172
	v_mfma_f32_16x16x32_f16 v[76:79], v[68:71], v[20:23], 0
	s_add_i32 m0, s33, 32768
	s_nop 0
	global_load_lds_dwordx4 v3, s[22:23]
	v_cvt_pkrtz_f16_f32 v72, v172, v173
	v_exp_f32_e32 v111, v111
	v_fmac_f32_e32 v174, v108, v173
	v_pk_mul_f16 v72, v56, v72
	v_fmac_f32_e32 v175, v109, v174
	v_exp_f32_e32 v112, v112
	v_cvt_pkrtz_f16_f32 v73, v174, v175
	v_fmac_f32_e32 v176, v110, v175
	v_pk_mul_f16 v73, v57, v73
	v_fmac_f32_e32 v177, v111, v176
	v_exp_f32_e32 v113, v113
	v_cvt_pkrtz_f16_f32 v74, v176, v177
	v_fmac_f32_e32 v178, v112, v177
	v_pk_mul_f16 v74, v58, v74
	s_waitcnt lgkmcnt(2)
	v_add_f32_e32 v200, v85, v90
	v_fmac_f32_e32 v179, v113, v178
	v_add_f32_e32 v88, v84, v89
	v_cvt_pkrtz_f16_f32 v75, v178, v179
	v_pk_mul_f16 v75, v59, v75
	v_exp_f32_e32 v114, v114
	v_exp_f32_e32 v115, v115
	v_mfma_f32_16x16x32_f16 v[76:79], v[72:75], v[24:27], v[76:79]
	s_mov_b32 m0, s34
	ds_read_b128 v[52:55], v93 offset:32768
	global_load_lds_dwordx4 v4, s[20:21]
	ds_bpermute_b32 v90, v87, v88
	s_waitcnt lgkmcnt(2)
	v_exp_f32_e32 v116, v116
	v_exp_f32_e32 v117, v117
	v_mfma_f32_32x32x16_f16 v[98:113], v[32:35], v[28:31], 0
	ds_read_u16 v32, v10 offset:32
	s_add_i32 m0, s34, 32768
	ds_read_b128 v[56:59], v93 offset:33792
	global_load_lds_dwordx4 v4, s[22:23]
	v_fmac_f32_e32 v148, v114, v179
	v_exp_f32_e32 v118, v118
	v_fmac_f32_e32 v149, v115, v148
	v_exp_f32_e32 v119, v119
	v_fmac_f32_e32 v150, v116, v149
	v_cvt_pkrtz_f16_f32 v68, v148, v149
	v_exp_f32_e32 v120, v120
	v_fmac_f32_e32 v151, v117, v150
	v_pk_mul_f16 v68, v204, v68
	v_exp_f32_e32 v121, v121
	v_add_f32_e32 v84, v76, v77
	v_add_f32_e32 v91, v78, v79
	v_fmac_f32_e32 v152, v118, v151
	v_add_f32_e32 v84, v84, v91
	v_cvt_pkrtz_f16_f32 v69, v150, v151
	v_mfma_f32_32x32x16_f16 v[132:147], v[36:39], v[44:47], 0
	ds_read_b128 v[44:47], v93 offset:2048
	ds_bpermute_b32 v89, v86, v84
	s_cmp_eq_u32 s40, 0
	s_cselect_b64 s[56:57], 0, s[42:43]
	s_and_saveexec_b64 s[44:45], s[56:57]
	global_store_dword v[16:17], v201, off offset:-192 sc1
	global_store_dword v[16:17], v202, off offset:-128 sc1
	global_store_dword v[16:17], v203, off offset:-64 sc1
	s_and_b64 exec, s[44:45], s[42:43]
	global_store_dword v[16:17], v196, off sc1
	global_store_dword v[16:17], v197, off offset:64 sc1
	global_store_dword v[16:17], v198, off offset:128 sc1
	global_store_dword v[16:17], v199, off offset:192 sc1
	global_store_dword v[16:17], v200, off offset:256 sc1
	s_mov_b64 exec, s[44:45]
	v_exp_f32_e32 v122, v122
	v_fmac_f32_e32 v153, v119, v152
	v_pk_mul_f16 v69, v205, v69
	v_exp_f32_e32 v123, v123
	v_fmac_f32_e32 v154, v120, v153
	v_cvt_pkrtz_f16_f32 v70, v152, v153
	v_exp_f32_e32 v124, v124
	v_fmac_f32_e32 v155, v121, v154
	v_pk_mul_f16 v70, v206, v70
	v_exp_f32_e32 v125, v125
	v_mfma_f32_32x32x16_f16 v[164:179], v[36:39], v[48:51], 0
	ds_read_b128 v[36:39], v13 offset:256
	s_mov_b32 m0, s35
	ds_read_b128 v[48:51], v93 offset:3072
	global_load_lds_dwordx4 v5, s[20:21]
	s_add_i32 m0, s35, 32768
	s_nop 0
	global_load_lds_dwordx4 v5, s[22:23]
	v_cvt_pkrtz_f16_f32 v71, v154, v155
	v_fmac_f32_e32 v188, v122, v155
	v_pk_mul_f16 v71, v207, v71
	v_exp_f32_e32 v126, v126
	v_fmac_f32_e32 v189, v123, v188
	v_mfma_f32_16x16x32_f16 v[80:83], v[68:71], v[20:23], 0
	s_mov_b32 m0, s29
	s_nop 0
	global_load_lds_dword v6, s[24:25]
	global_load_ushort v18, v7, s[26:27]
	global_load_ushort v19, v7, s[26:27] offset:128
	v_cvt_pkrtz_f16_f32 v72, v188, v189
	v_exp_f32_e32 v127, v127
	v_fmac_f32_e32 v190, v124, v189
	v_pk_mul_f16 v72, v208, v72
	v_fmac_f32_e32 v191, v125, v190
	v_exp_f32_e32 v128, v128
	v_cvt_pkrtz_f16_f32 v73, v190, v191
	v_fmac_f32_e32 v192, v126, v191
	v_pk_mul_f16 v73, v209, v73
	v_fmac_f32_e32 v193, v127, v192
	v_exp_f32_e32 v129, v129
	v_cvt_pkrtz_f16_f32 v74, v192, v193
	v_fmac_f32_e32 v194, v128, v193
	v_pk_mul_f16 v74, v210, v74
	s_waitcnt lgkmcnt(2)
	v_add_f32_e32 v201, v88, v90
	v_fmac_f32_e32 v195, v129, v194
	v_add_f32_e32 v85, v84, v89
	v_cvt_pkrtz_f16_f32 v75, v194, v195
	s_cmp_lt_u32 s40, 29
	s_cselect_b32 s58, 0x4000, 0
	s_cselect_b32 s59, 0x100, 0
	s_add_u32 s20, s20, s58
	s_addc_u32 s21, s21, 0
	s_add_u32 s22, s22, s58
	s_addc_u32 s23, s23, 0
	s_add_u32 s24, s24, s59
	s_addc_u32 s25, s25, 0
	s_add_u32 s26, s26, s59
	s_addc_u32 s27, s27, 0
	v_pk_mul_f16 v75, v211, v75
	v_lshl_add_u64 v[16:17], v[16:17], 0, s[46:47]
	v_swap_b32 v92, v93
	v_swap_b32 v9, v10
	v_swap_b32 v11, v13
	v_swap_b32 v8, v94
	s_xor_b32 s32, s32, 0x4000
	s_xor_b32 s33, s33, 0x4000
	s_xor_b32 s34, s34, 0x4000
	s_xor_b32 s35, s35, 0x4000
	s_xor_b32 s29, s29, 0x100
	s_add_u32 s40, s40, 1
	s_cmp_lt_u32 s40, 32
	s_cbranch_scc1 .Lscan_loop
	s_nop 1
	v_mfma_f32_16x16x32_f16 v[80:83], v[72:75], v[24:27], v[80:83]
	ds_bpermute_b32 v90, v87, v85
	s_nop 15
	v_add_f32_e32 v84, v80, v81
	v_add_f32_e32 v91, v82, v83
	s_nop 0
	v_add_f32_e32 v84, v84, v91
	s_waitcnt lgkmcnt(0)
	v_add_f32_e32 v202, v85, v90
	ds_bpermute_b32 v89, v86, v84
	s_waitcnt lgkmcnt(0)
	v_add_f32_e32 v88, v84, v89
	s_nop 0
	ds_bpermute_b32 v90, v87, v88
	s_waitcnt lgkmcnt(0)
	v_add_f32_e32 v203, v88, v90
	s_nop 1
	s_and_saveexec_b64 s[44:45], s[42:43]
	global_store_dword v[16:17], v201, off offset:-192 sc1
	global_store_dword v[16:17], v202, off offset:-128 sc1
	global_store_dword v[16:17], v203, off offset:-64 sc1
	s_waitcnt vmcnt(0)
	s_endpgm
